# v48 assignment with the converter copies' LDS read chain de-serialised (32 reads then one wait)
# speedup vs baseline: 1.0055x; 1.0055x over previous
; __device__ __forceinline__ void conv_load(const ConvItem& ci, int lane, float (&v)[64]) {
;     const bool okc = ci.srcc >= 0 && (ci.srcc + lane) < ci.ncols;
;     const float* base = ci.W + (okc ? ci.srcc + lane : 0);
;     const int kmax = ci.Ksrc - 1;
; #pragma unroll
;     for (int i = 0; i < 64; ++i) { const int k = ci.k0 + i, kk = k < kmax ? k : kmax; v[i] = __builtin_nontemporal_load(base + (size_t)kk * ci.ldw); }
; #pragma unroll
;     for (int i = 0; i < 64; ++i) v[i] = (okc && (ci.k0 + i) < ci.Ksrc) ? v[i] : 0.f;
.Lcvp11_30:
	s_cmp_lt_i32 s58, s76
	s_cselect_b64 s[4:5], -1, 0
	s_and_b64 s[4:5], vcc, s[4:5]
	s_cmp_lt_i32 s64, s76
	s_waitcnt vmcnt(62)
	v_cndmask_b32_e64 v21, 0, v21, s[4:5]
	s_cselect_b64 s[4:5], -1, 0
	s_and_b64 s[4:5], vcc, s[4:5]
	s_cmp_lt_i32 s65, s76
	v_cndmask_b32_e64 v20, 0, v20, s[4:5]
	s_cselect_b64 s[4:5], -1, 0
	s_and_b64 s[4:5], vcc, s[4:5]
	s_cmp_lt_i32 s78, s76
	s_waitcnt vmcnt(61)
	v_cndmask_b32_e64 v19, 0, v19, s[4:5]
	s_cselect_b64 s[4:5], -1, 0
	s_and_b64 s[4:5], vcc, s[4:5]
	s_cmp_lt_i32 s79, s76
	s_waitcnt vmcnt(60)
	v_cndmask_b32_e64 v18, 0, v18, s[4:5]
	s_cselect_b64 s[4:5], -1, 0
	s_and_b64 s[4:5], vcc, s[4:5]
	s_cmp_lt_i32 s80, s76
	s_waitcnt vmcnt(59)
	v_cndmask_b32_e64 v17, 0, v17, s[4:5]
	s_cselect_b64 s[4:5], -1, 0
	s_and_b64 s[4:5], vcc, s[4:5]
	s_cmp_lt_i32 s81, s76
	s_waitcnt vmcnt(58)
	v_cndmask_b32_e64 v16, 0, v16, s[4:5]
	s_cselect_b64 s[4:5], -1, 0
	s_and_b64 s[4:5], vcc, s[4:5]
	s_cmp_lt_i32 s82, s76
	s_waitcnt vmcnt(57)
	v_cndmask_b32_e64 v15, 0, v15, s[4:5]
	s_cselect_b64 s[4:5], -1, 0
	s_and_b64 s[4:5], vcc, s[4:5]
	s_cmp_lt_i32 s83, s76
	s_waitcnt vmcnt(56)
	v_cndmask_b32_e64 v8, 0, v8, s[4:5]
	s_cselect_b64 s[4:5], -1, 0
	s_and_b64 s[4:5], vcc, s[4:5]
	s_cmp_lt_i32 s85, s76
	s_waitcnt vmcnt(55)
	v_cndmask_b32_e64 v29, 0, v29, s[4:5]
	s_cselect_b64 s[4:5], -1, 0
	s_and_b64 s[4:5], vcc, s[4:5]
	s_cmp_lt_i32 s86, s76
	s_waitcnt vmcnt(54)
	v_cndmask_b32_e64 v28, 0, v28, s[4:5]
	s_cselect_b64 s[4:5], -1, 0
	s_and_b64 s[4:5], vcc, s[4:5]
	s_cmp_lt_i32 s87, s76
	s_waitcnt vmcnt(53)
	v_cndmask_b32_e64 v27, 0, v27, s[4:5]
	s_cselect_b64 s[4:5], -1, 0
	s_and_b64 s[4:5], vcc, s[4:5]
	s_cmp_lt_i32 s88, s76
	s_waitcnt vmcnt(52)
	v_cndmask_b32_e64 v26, 0, v26, s[4:5]
	s_cselect_b64 s[4:5], -1, 0
	s_and_b64 s[4:5], vcc, s[4:5]
	s_cmp_lt_i32 s89, s76
	s_waitcnt vmcnt(51)
	v_cndmask_b32_e64 v25, 0, v25, s[4:5]
	s_cselect_b64 s[4:5], -1, 0
	s_and_b64 s[4:5], vcc, s[4:5]
	s_cmp_lt_i32 s90, s76
	s_waitcnt vmcnt(50)
	v_cndmask_b32_e64 v24, 0, v24, s[4:5]
	s_cselect_b64 s[4:5], -1, 0
	s_and_b64 s[4:5], vcc, s[4:5]
	s_cmp_lt_i32 s92, s76
	s_waitcnt vmcnt(49)
	v_cndmask_b32_e64 v23, 0, v23, s[4:5]
	s_cselect_b64 s[4:5], -1, 0
	s_and_b64 s[4:5], vcc, s[4:5]
	s_cmp_lt_i32 s93, s76
	s_waitcnt vmcnt(48)
	v_cndmask_b32_e64 v22, 0, v22, s[4:5]
	s_cselect_b64 s[4:5], -1, 0
	s_and_b64 s[4:5], vcc, s[4:5]
	s_cmp_lt_i32 s94, s76
	s_waitcnt vmcnt(47)
	v_cndmask_b32_e64 v37, 0, v37, s[4:5]
	s_cselect_b64 s[4:5], -1, 0
	s_and_b64 s[4:5], vcc, s[4:5]
	s_cmp_lt_i32 s95, s76
	s_waitcnt vmcnt(46)
	v_cndmask_b32_e64 v36, 0, v36, s[4:5]
	s_cselect_b64 s[4:5], -1, 0
	s_and_b64 s[4:5], vcc, s[4:5]
	s_cmp_lt_i32 s50, s76
	s_waitcnt vmcnt(45)
	v_cndmask_b32_e64 v35, 0, v35, s[4:5]
	s_cselect_b64 s[4:5], -1, 0
	s_and_b64 s[4:5], vcc, s[4:5]
	s_cmp_lt_i32 s51, s76
	s_waitcnt vmcnt(44)
	v_cndmask_b32_e64 v34, 0, v34, s[4:5]
	s_cselect_b64 s[4:5], -1, 0
	s_and_b64 s[4:5], vcc, s[4:5]
	s_cmp_lt_i32 s52, s76
	s_waitcnt vmcnt(43)
	v_cndmask_b32_e64 v33, 0, v33, s[4:5]
	s_cselect_b64 s[4:5], -1, 0
	s_and_b64 s[4:5], vcc, s[4:5]
	s_cmp_lt_i32 s53, s76
	s_waitcnt vmcnt(42)
	v_cndmask_b32_e64 v32, 0, v32, s[4:5]
	s_cselect_b64 s[4:5], -1, 0
	s_and_b64 s[4:5], vcc, s[4:5]
	s_cmp_lt_i32 s6, s76
	s_waitcnt vmcnt(41)
	v_cndmask_b32_e64 v31, 0, v31, s[4:5]
	s_cselect_b64 s[4:5], -1, 0
	s_and_b64 s[4:5], vcc, s[4:5]
	s_cmp_lt_i32 s7, s76
	s_waitcnt vmcnt(40)
	v_cndmask_b32_e64 v30, 0, v30, s[4:5]
	s_cselect_b64 s[4:5], -1, 0
	s_and_b64 s[4:5], vcc, s[4:5]
	s_cmp_lt_i32 s8, s76
	s_waitcnt vmcnt(39)
	v_cndmask_b32_e64 v45, 0, v45, s[4:5]
	s_cselect_b64 s[4:5], -1, 0
	s_and_b64 s[4:5], vcc, s[4:5]
	s_cmp_lt_i32 s9, s76
	s_waitcnt vmcnt(38)
	v_cndmask_b32_e64 v44, 0, v44, s[4:5]
	s_cselect_b64 s[4:5], -1, 0
	s_and_b64 s[4:5], vcc, s[4:5]
	s_cmp_lt_i32 s10, s76
	s_waitcnt vmcnt(37)
	v_cndmask_b32_e64 v43, 0, v43, s[4:5]
	s_cselect_b64 s[4:5], -1, 0
	s_and_b64 s[4:5], vcc, s[4:5]
	s_cmp_lt_i32 s11, s76
	s_waitcnt vmcnt(36)
	v_cndmask_b32_e64 v42, 0, v42, s[4:5]
	s_cselect_b64 s[4:5], -1, 0
	s_and_b64 s[4:5], vcc, s[4:5]
	s_cmp_lt_i32 s14, s76
	s_waitcnt vmcnt(35)
	v_cndmask_b32_e64 v41, 0, v41, s[4:5]
	s_cselect_b64 s[4:5], -1, 0
	s_and_b64 s[4:5], vcc, s[4:5]
	s_cmp_lt_i32 s15, s76
	s_waitcnt vmcnt(34)
	v_cndmask_b32_e64 v40, 0, v40, s[4:5]
	s_cselect_b64 s[4:5], -1, 0
	s_and_b64 s[4:5], vcc, s[4:5]
	s_cmp_lt_i32 s16, s76
	s_waitcnt vmcnt(33)
	v_cndmask_b32_e64 v39, 0, v39, s[4:5]
	s_cselect_b64 s[4:5], -1, 0
	s_and_b64 s[4:5], vcc, s[4:5]
	s_cmp_lt_i32 s17, s76
	s_waitcnt vmcnt(32)
	v_cndmask_b32_e64 v38, 0, v38, s[4:5]
	s_cselect_b64 s[4:5], -1, 0
	s_and_b64 s[4:5], vcc, s[4:5]
	s_cmp_lt_i32 s12, s76
	s_waitcnt vmcnt(31)
	v_cndmask_b32_e64 v53, 0, v53, s[4:5]
	s_cselect_b64 s[4:5], -1, 0
	s_and_b64 s[4:5], vcc, s[4:5]
	s_cmp_lt_i32 s13, s76
	s_waitcnt vmcnt(30)
	v_cndmask_b32_e64 v52, 0, v52, s[4:5]
	s_cselect_b64 s[4:5], -1, 0
	s_and_b64 s[4:5], vcc, s[4:5]
	s_cmp_lt_i32 s20, s76
	s_waitcnt vmcnt(29)
	v_cndmask_b32_e64 v51, 0, v51, s[4:5]
	s_cselect_b64 s[4:5], -1, 0
	s_and_b64 s[4:5], vcc, s[4:5]
	s_cmp_lt_i32 s21, s76
	s_waitcnt vmcnt(28)
	v_cndmask_b32_e64 v50, 0, v50, s[4:5]
	s_cselect_b64 s[4:5], -1, 0
	s_and_b64 s[4:5], vcc, s[4:5]
	s_cmp_lt_i32 s24, s76
	s_waitcnt vmcnt(27)
	v_cndmask_b32_e64 v49, 0, v49, s[4:5]
	s_cselect_b64 s[4:5], -1, 0
	s_and_b64 s[4:5], vcc, s[4:5]
	s_cmp_lt_i32 s25, s76
	s_waitcnt vmcnt(26)
	v_cndmask_b32_e64 v48, 0, v48, s[4:5]
	s_cselect_b64 s[4:5], -1, 0
	s_and_b64 s[4:5], vcc, s[4:5]
	s_cmp_lt_i32 s26, s76
	s_waitcnt vmcnt(25)
	v_cndmask_b32_e64 v47, 0, v47, s[4:5]
	s_cselect_b64 s[4:5], -1, 0
	s_and_b64 s[4:5], vcc, s[4:5]
	s_cmp_lt_i32 s27, s76
	s_waitcnt vmcnt(24)
; #define LAS __attribute__((address_space(3)))
; #define LDS_WAIT() asm volatile("s_waitcnt lgkmcnt(0)" ::: "memory")
; __device__ __forceinline__ void conv_load(const ConvItem& ci, int lane, float (&v)[64]) {
;     ...
;     for (int i = 0; i < 64; ++i) v[i] = (okc && (ci.k0 + i) < ci.Ksrc) ? v[i] : 0.f;
; }
; __device__ __forceinline__ void conv_store(const ConvItem& ci, LAS float* scr, int lane, const float (&v)[64]) {
;     const int c = lane & 7;
;     f32x4 s0 = {1.f, 1.f, 1.f, 1.f}, s1 = s0;
;     if (ci.ks) { const int kb = ci.k0 + 8 * c < ci.Ksrc - 8 ? ci.k0 + 8 * c : ci.Ksrc - 8; s0 = *(const f32x4*)(ci.ks + kb); s1 = *(const f32x4*)(ci.ks + kb + 4); }
; #pragma unroll
;     for (int i = 0; i < 64; ++i) scr[i * 65 + lane] = v[i];
;     LDS_WAIT(); asm volatile("" ::: "memory");
	v_cndmask_b32_e64 v46, 0, v46, s[4:5]
	s_cselect_b64 s[4:5], -1, 0
	s_and_b64 s[4:5], vcc, s[4:5]
	s_cmp_lt_i32 s18, s76
	s_waitcnt vmcnt(23)
	v_cndmask_b32_e64 v61, 0, v61, s[4:5]
	s_cselect_b64 s[4:5], -1, 0
	s_and_b64 s[4:5], vcc, s[4:5]
	s_cmp_lt_i32 s19, s76
	s_waitcnt vmcnt(22)
	v_cndmask_b32_e64 v60, 0, v60, s[4:5]
	s_cselect_b64 s[4:5], -1, 0
	s_and_b64 s[4:5], vcc, s[4:5]
	s_cmp_lt_i32 s28, s76
	s_waitcnt vmcnt(21)
	v_cndmask_b32_e64 v59, 0, v59, s[4:5]
	s_cselect_b64 s[4:5], -1, 0
	s_and_b64 s[4:5], vcc, s[4:5]
	s_cmp_lt_i32 s29, s76
	s_waitcnt vmcnt(20)
	v_cndmask_b32_e64 v58, 0, v58, s[4:5]
	s_cselect_b64 s[4:5], -1, 0
	s_and_b64 s[4:5], vcc, s[4:5]
	s_cmp_lt_i32 s22, s76
	s_waitcnt vmcnt(19)
	v_cndmask_b32_e64 v57, 0, v57, s[4:5]
	s_cselect_b64 s[4:5], -1, 0
	s_and_b64 s[4:5], vcc, s[4:5]
	s_cmp_lt_i32 s23, s76
	s_waitcnt vmcnt(18)
	v_cndmask_b32_e64 v56, 0, v56, s[4:5]
	s_cselect_b64 s[4:5], -1, 0
	s_and_b64 s[4:5], vcc, s[4:5]
	s_cmp_lt_i32 s30, s76
	s_waitcnt vmcnt(17)
	v_cndmask_b32_e64 v55, 0, v55, s[4:5]
	s_cselect_b64 s[4:5], -1, 0
	s_and_b64 s[4:5], vcc, s[4:5]
	s_cmp_lt_i32 s31, s76
	s_waitcnt vmcnt(16)
	v_cndmask_b32_e64 v54, 0, v54, s[4:5]
	s_cselect_b64 s[4:5], -1, 0
	s_and_b64 s[4:5], vcc, s[4:5]
	s_cmp_lt_i32 s36, s76
	s_waitcnt vmcnt(15)
	v_cndmask_b32_e64 v70, 0, v70, s[4:5]
	s_cselect_b64 s[4:5], -1, 0
	s_and_b64 s[4:5], vcc, s[4:5]
	s_cmp_lt_i32 s37, s76
	s_waitcnt vmcnt(14)
	v_cndmask_b32_e64 v69, 0, v69, s[4:5]
	s_cselect_b64 s[4:5], -1, 0
	s_and_b64 s[4:5], vcc, s[4:5]
	s_cmp_lt_i32 s38, s76
	s_waitcnt vmcnt(13)
	v_cndmask_b32_e64 v68, 0, v68, s[4:5]
	s_cselect_b64 s[4:5], -1, 0
	s_and_b64 s[4:5], vcc, s[4:5]
	s_cmp_lt_i32 s39, s76
	s_waitcnt vmcnt(12)
	v_cndmask_b32_e64 v67, 0, v67, s[4:5]
	s_cselect_b64 s[4:5], -1, 0
	s_and_b64 s[4:5], vcc, s[4:5]
	s_cmp_lt_i32 s34, s76
	s_waitcnt vmcnt(11)
	v_cndmask_b32_e64 v66, 0, v66, s[4:5]
	s_cselect_b64 s[4:5], -1, 0
	s_and_b64 s[4:5], vcc, s[4:5]
	s_cmp_lt_i32 s35, s76
	s_waitcnt vmcnt(10)
	v_cndmask_b32_e64 v64, 0, v64, s[4:5]
	s_cselect_b64 s[4:5], -1, 0
	s_and_b64 s[4:5], vcc, s[4:5]
	s_cmp_lt_i32 s42, s76
	s_waitcnt vmcnt(9)
	v_cndmask_b32_e64 v63, 0, v63, s[4:5]
	s_cselect_b64 s[4:5], -1, 0
	s_and_b64 s[4:5], vcc, s[4:5]
	s_cmp_lt_i32 s43, s76
	s_waitcnt vmcnt(8)
	v_cndmask_b32_e64 v62, 0, v62, s[4:5]
	s_cselect_b64 s[4:5], -1, 0
	s_and_b64 s[4:5], vcc, s[4:5]
	s_cmp_lt_i32 s54, s76
	s_waitcnt vmcnt(7)
	v_cndmask_b32_e64 v65, 0, v65, s[4:5]
	s_cselect_b64 s[4:5], -1, 0
	s_and_b64 s[4:5], vcc, s[4:5]
	s_cmp_lt_i32 s55, s76
	s_waitcnt vmcnt(6)
	v_cndmask_b32_e64 v74, 0, v74, s[4:5]
	s_cselect_b64 s[4:5], -1, 0
	s_and_b64 s[4:5], vcc, s[4:5]
	s_cmp_lt_i32 s46, s76
	ds_write2_b32 v12, v21, v20 offset1:65
	ds_write2_b32 v12, v19, v18 offset0:130 offset1:195
	v_add_u32_e32 v18, 0x400, v12
	s_waitcnt vmcnt(5)
	v_cndmask_b32_e64 v73, 0, v73, s[4:5]
	s_cselect_b64 s[4:5], -1, 0
	ds_write2_b32 v18, v17, v16 offset0:4 offset1:69
	ds_write2_b32 v18, v15, v8 offset0:134 offset1:199
	v_add_u32_e32 v8, 0x800, v12
	s_and_b64 s[4:5], vcc, s[4:5]
	ds_write2_b32 v8, v29, v28 offset0:8 offset1:73
	ds_write2_b32 v8, v27, v26 offset0:138 offset1:203
	v_add_u32_e32 v8, 0xc00, v12
	s_cmp_lt_i32 s47, s76
	ds_write2_b32 v8, v25, v24 offset0:12 offset1:77
	ds_write2_b32 v8, v23, v22 offset0:142 offset1:207
	v_add_u32_e32 v8, 0x1000, v12
	s_waitcnt vmcnt(4)
	v_cndmask_b32_e64 v72, 0, v72, s[4:5]
	s_cselect_b64 s[4:5], -1, 0
	ds_write2_b32 v8, v37, v36 offset0:16 offset1:81
	ds_write2_b32 v8, v35, v34 offset0:146 offset1:211
	v_add_u32_e32 v8, 0x1400, v12
	s_and_b64 s[4:5], vcc, s[4:5]
	ds_write2_b32 v8, v33, v32 offset0:20 offset1:85
	ds_write2_b32 v8, v31, v30 offset0:150 offset1:215
	v_add_u32_e32 v8, 0x1800, v12
	s_cmp_lt_i32 s48, s76
	ds_write2_b32 v8, v45, v44 offset0:24 offset1:89
	ds_write2_b32 v8, v43, v42 offset0:154 offset1:219
	v_add_u32_e32 v8, 0x1c00, v12
	s_waitcnt vmcnt(3)
	v_cndmask_b32_e64 v71, 0, v71, s[4:5]
	s_cselect_b64 s[4:5], -1, 0
	ds_write2_b32 v8, v41, v40 offset0:28 offset1:93
	ds_write2_b32 v8, v39, v38 offset0:158 offset1:223
	v_add_u32_e32 v8, 0x2000, v12
	s_and_b64 s[4:5], vcc, s[4:5]
	ds_write2_b32 v8, v53, v52 offset0:32 offset1:97
	ds_write2_b32 v8, v51, v50 offset0:162 offset1:227
	v_add_u32_e32 v8, 0x2400, v12
	s_cmp_lt_i32 s49, s76
	ds_write2_b32 v8, v49, v48 offset0:36 offset1:101
	ds_write2_b32 v8, v47, v46 offset0:166 offset1:231
	v_add_u32_e32 v8, 0x2800, v12
	s_waitcnt vmcnt(2)
	v_cndmask_b32_e64 v77, 0, v77, s[4:5]
	s_cselect_b64 s[4:5], -1, 0
	ds_write2_b32 v8, v61, v60 offset0:40 offset1:105
	ds_write2_b32 v8, v59, v58 offset0:170 offset1:235
	v_add_u32_e32 v8, 0x2c00, v12
	s_and_b64 s[4:5], vcc, s[4:5]
	ds_write2_b32 v8, v57, v56 offset0:44 offset1:109
	ds_write2_b32 v8, v55, v54 offset0:174 offset1:239
	v_add_u32_e32 v8, 0x3000, v12
	s_cmp_lt_i32 s44, s76
	ds_write2_b32 v8, v70, v69 offset0:48 offset1:113
	ds_write2_b32 v8, v68, v67 offset0:178 offset1:243
	v_add_u32_e32 v8, 0x3400, v12
	s_waitcnt vmcnt(1)
	v_cndmask_b32_e64 v76, 0, v76, s[4:5]
	s_cselect_b64 s[4:5], -1, 0
	ds_write2_b32 v8, v66, v64 offset0:52 offset1:117
	ds_write2_b32 v8, v63, v62 offset0:182 offset1:247
	v_add_u32_e32 v8, 0x3800, v12
	s_and_b64 vcc, vcc, s[4:5]
	ds_write2_b32 v8, v65, v74 offset0:56 offset1:121
	ds_write2_b32 v8, v73, v72 offset0:186 offset1:251
	v_add_u32_e32 v8, 0x3c00, v12
	s_waitcnt vmcnt(0)
	v_cndmask_b32_e32 v75, 0, v75, vcc
	ds_write2_b32 v8, v71, v77 offset0:60 offset1:125
	ds_write2_b32 v8, v76, v75 offset0:190 offset1:255
	s_waitcnt lgkmcnt(0)
; __device__ __forceinline__ unsigned cvt_pk_bf16(float lo, float hi) { unsigned r; asm volatile("v_cvt_pk_bf16_f32 %0, %1, %2" : "=v"(r) : "v"(lo), "v"(hi)); return r; }
; #define LAS __attribute__((address_space(3)))
; #define LDS_WAIT() asm volatile("s_waitcnt lgkmcnt(0)" ::: "memory")
; __device__ __forceinline__ void conv_store(const ConvItem& ci, LAS float* scr, int lane, const float (&v)[64]) {
;     ...
;     LDS_WAIT(); asm volatile("" ::: "memory");
; #pragma unroll
;     for (int j = 0; j < 8; ++j) { const int n = (lane >> 3) + 8 * j; const LAS float* s = scr + (8 * c) * 65 + n;
;         v4u o; o.x = cvt_pk_bf16(s[0 * 65] * s0[0], s[1 * 65] * s0[1]); o.y = cvt_pk_bf16(s[2 * 65] * s0[2], s[3 * 65] * s0[3]); o.z = cvt_pk_bf16(s[4 * 65] * s1[0], s[5 * 65] * s1[1]); o.w = cvt_pk_bf16(s[6 * 65] * s1[2], s[7 * 65] * s1[3]);
;         *(v4u*)(ci.dst + (size_t)(ci.drow0 + n) * ci.ldd + ci.k0 + 8 * c) = o; }
	v_add_u32_e32 v192, 0x400, v14
	ds_read2_b32 v[128:129], v14 offset1:65
	ds_read2_b32 v[130:131], v14 offset0:130 offset1:195
	ds_read2_b32 v[132:133], v192 offset0:4 offset1:69
	ds_read2_b32 v[134:135], v192 offset0:134 offset1:199
	ds_read2_b32 v[136:137], v14 offset0:8 offset1:73
	ds_read2_b32 v[138:139], v14 offset0:138 offset1:203
	ds_read2_b32 v[140:141], v192 offset0:12 offset1:77
	ds_read2_b32 v[142:143], v192 offset0:142 offset1:207
	ds_read2_b32 v[144:145], v14 offset0:16 offset1:81
	ds_read2_b32 v[146:147], v14 offset0:146 offset1:211
	ds_read2_b32 v[148:149], v192 offset0:20 offset1:85
	ds_read2_b32 v[150:151], v192 offset0:150 offset1:215
	ds_read2_b32 v[152:153], v14 offset0:24 offset1:89
	ds_read2_b32 v[154:155], v14 offset0:154 offset1:219
	ds_read2_b32 v[156:157], v192 offset0:28 offset1:93
	ds_read2_b32 v[158:159], v192 offset0:158 offset1:223
	ds_read2_b32 v[160:161], v14 offset0:32 offset1:97
	ds_read2_b32 v[162:163], v14 offset0:162 offset1:227
	ds_read2_b32 v[164:165], v192 offset0:36 offset1:101
	ds_read2_b32 v[166:167], v192 offset0:166 offset1:231
	ds_read2_b32 v[168:169], v14 offset0:40 offset1:105
	ds_read2_b32 v[170:171], v14 offset0:170 offset1:235
	ds_read2_b32 v[172:173], v192 offset0:44 offset1:109
	ds_read2_b32 v[174:175], v192 offset0:174 offset1:239
	ds_read2_b32 v[176:177], v14 offset0:48 offset1:113
	ds_read2_b32 v[178:179], v14 offset0:178 offset1:243
	ds_read2_b32 v[180:181], v192 offset0:52 offset1:117
	ds_read2_b32 v[182:183], v192 offset0:182 offset1:247
	ds_read2_b32 v[184:185], v14 offset0:56 offset1:121
	ds_read2_b32 v[186:187], v14 offset0:186 offset1:251
	ds_read2_b32 v[188:189], v192 offset0:60 offset1:125
	ds_read2_b32 v[190:191], v192 offset0:190 offset1:255
	s_waitcnt lgkmcnt(0)
	v_add_u32_e32 v24, s59, v13
	v_mul_lo_u32 v22, s57, v24
	s_ashr_i32 s59, s58, 31
	v_readlane_b32 s76, v254, 31
	s_waitcnt lgkmcnt(0)
	v_mul_f32_e32 v8, v4, v128
	v_mul_f32_e32 v15, v5, v129
	v_cvt_pk_bf16_f32 v16, v8, v15
	s_add_i32 s3, s3, s33
	s_add_i32 s66, s66, s67
	s_add_i32 s68, s68, s69
	s_add_i32 s70, s70, s71
	s_waitcnt lgkmcnt(0)
	v_mul_f32_e32 v15, v7, v131
	v_mul_f32_e32 v8, v6, v130
	v_cvt_pk_bf16_f32 v17, v8, v15
	v_add_u32_e32 v15, 0x400, v14
	s_add_i32 s72, s72, s73
	s_add_i32 s74, s74, s75
	v_readlane_b32 s78, v254, 33
	v_readlane_b32 s79, v254, 34
	s_waitcnt lgkmcnt(0)
	v_mul_f32_e32 v8, v0, v132
	v_mul_f32_e32 v18, v1, v133
	v_cvt_pk_bf16_f32 v18, v8, v18
	v_readlane_b32 s80, v255, 21
	v_readlane_b32 s77, v254, 32
	s_movk_i32 s78, 0x1580
	v_readlane_b32 s82, v255, 23
	s_waitcnt lgkmcnt(0)
	v_mul_f32_e32 v8, v2, v134
	v_mul_f32_e32 v19, v3, v135
	v_cvt_pk_bf16_f32 v19, v8, v19
	v_ashrrev_i32_e32 v8, 31, v24
	v_mul_lo_u32 v8, s56, v8
	v_mad_u64_u32 v[20:21], s[4:5], s56, v24, 0
	v_add3_u32 v21, v21, v8, v22
	v_lshl_add_u64 v[20:21], v[20:21], 1, s[60:61]
	s_lshl_b64 s[4:5], s[58:59], 1
	v_lshl_add_u64 v[20:21], v[20:21], 0, s[4:5]
	v_lshlrev_b32_e32 v8, 1, v10
	v_lshl_add_u64 v[20:21], v[20:21], 0, v[8:9]
	global_store_dwordx4 v[20:21], v[16:19], off
	s_cmpk_lt_i32 s3, 26496
	v_readlane_b32 s83, v255, 24
	s_waitcnt lgkmcnt(0)
	v_mul_f32_e32 v16, v4, v136
	v_mul_f32_e32 v17, v5, v137
	v_cvt_pk_bf16_f32 v16, v16, v17
	s_mov_b32 s79, 0x3f22f983
	s_mov_b32 s85, 0xbfc90fda
	s_brev_b32 s86, 1
	s_movk_i32 s87, 0x1f8
	s_waitcnt lgkmcnt(0)
	v_mul_f32_e32 v17, v6, v138
	v_mul_f32_e32 v18, v7, v139
	v_cvt_pk_bf16_f32 v17, v17, v18
	s_mov_b64 s[88:89], 0x80
	s_mov_b64 s[92:93], 0x4000
	s_mov_b64 s[94:95], 0x4800
	v_readlane_b32 s81, v255, 22
	s_waitcnt lgkmcnt(0)
	v_mul_f32_e32 v18, v0, v140
	v_mul_f32_e32 v19, v1, v141
	v_cvt_pk_bf16_f32 v18, v18, v19
	s_waitcnt lgkmcnt(0)
	v_mul_f32_e32 v19, v2, v142
	v_mul_f32_e32 v20, v3, v143
	v_cvt_pk_bf16_f32 v19, v19, v20
	v_add_u32_e32 v20, 8, v24
	v_ashrrev_i32_e32 v21, 31, v20
	v_mul_lo_u32 v22, s56, v21
	v_mul_lo_u32 v23, s57, v20
	v_mad_u64_u32 v[20:21], s[6:7], s56, v20, 0
	v_add3_u32 v21, v21, v22, v23
	v_lshl_add_u64 v[20:21], v[20:21], 1, s[60:61]
	v_lshl_add_u64 v[20:21], v[20:21], 0, s[4:5]
	v_lshl_add_u64 v[20:21], v[20:21], 0, v[8:9]
	global_store_dwordx4 v[20:21], v[16:19], off
	s_waitcnt lgkmcnt(0)
	s_nop 0
	v_mul_f32_e32 v16, v4, v144
	v_mul_f32_e32 v17, v5, v145
	v_cvt_pk_bf16_f32 v16, v16, v17
	s_waitcnt lgkmcnt(0)
	v_mul_f32_e32 v17, v6, v146
	v_mul_f32_e32 v18, v7, v147
	v_cvt_pk_bf16_f32 v17, v17, v18
	s_waitcnt lgkmcnt(0)
	v_mul_f32_e32 v18, v0, v148
	v_mul_f32_e32 v19, v1, v149
	v_cvt_pk_bf16_f32 v18, v18, v19
	s_waitcnt lgkmcnt(0)
; __device__ __forceinline__ unsigned cvt_pk_bf16(float lo, float hi) { unsigned r; asm volatile("v_cvt_pk_bf16_f32 %0, %1, %2" : "=v"(r) : "v"(lo), "v"(hi)); return r; }
; #define LAS __attribute__((address_space(3)))
; #define LDS_WAIT() asm volatile("s_waitcnt lgkmcnt(0)" ::: "memory")
; __device__ __forceinline__ void conv_store(const ConvItem& ci, LAS float* scr, int lane, const float (&v)[64]) {
;     ...
;     for (int j = 0; j < 8; ++j) { const int n = (lane >> 3) + 8 * j; const LAS float* s = scr + (8 * c) * 65 + n;
;         v4u o; o.x = cvt_pk_bf16(s[0 * 65] * s0[0], s[1 * 65] * s0[1]); o.y = cvt_pk_bf16(s[2 * 65] * s0[2], s[3 * 65] * s0[3]); o.z = cvt_pk_bf16(s[4 * 65] * s1[0], s[5 * 65] * s1[1]); o.w = cvt_pk_bf16(s[6 * 65] * s1[2], s[7 * 65] * s1[3]);
;         *(v4u*)(ci.dst + (size_t)(ci.drow0 + n) * ci.ldd + ci.k0 + 8 * c) = o; }
;     LDS_WAIT(); asm volatile("" ::: "memory");
	v_mul_f32_e32 v19, v2, v150
	v_mul_f32_e32 v20, v3, v151
	v_cvt_pk_bf16_f32 v19, v19, v20
	v_add_u32_e32 v20, 16, v24
	v_ashrrev_i32_e32 v21, 31, v20
	v_mul_lo_u32 v22, s56, v21
	v_mul_lo_u32 v23, s57, v20
	v_mad_u64_u32 v[20:21], s[6:7], s56, v20, 0
	v_add3_u32 v21, v21, v22, v23
	v_lshl_add_u64 v[20:21], v[20:21], 1, s[60:61]
	v_lshl_add_u64 v[20:21], v[20:21], 0, s[4:5]
	v_lshl_add_u64 v[20:21], v[20:21], 0, v[8:9]
	global_store_dwordx4 v[20:21], v[16:19], off
	s_waitcnt lgkmcnt(0)
	s_nop 0
	v_mul_f32_e32 v16, v4, v152
	v_mul_f32_e32 v17, v5, v153
	v_cvt_pk_bf16_f32 v16, v16, v17
	s_waitcnt lgkmcnt(0)
	v_mul_f32_e32 v17, v6, v154
	v_mul_f32_e32 v18, v7, v155
	v_cvt_pk_bf16_f32 v17, v17, v18
	s_waitcnt lgkmcnt(0)
	v_mul_f32_e32 v18, v0, v156
	v_mul_f32_e32 v19, v1, v157
	v_cvt_pk_bf16_f32 v18, v18, v19
	s_waitcnt lgkmcnt(0)
	v_mul_f32_e32 v19, v2, v158
	v_mul_f32_e32 v20, v3, v159
	v_cvt_pk_bf16_f32 v19, v19, v20
	v_add_u32_e32 v20, 24, v24
	v_ashrrev_i32_e32 v21, 31, v20
	v_mul_lo_u32 v22, s56, v21
	v_mul_lo_u32 v23, s57, v20
	v_mad_u64_u32 v[20:21], s[6:7], s56, v20, 0
	v_add3_u32 v21, v21, v22, v23
	v_lshl_add_u64 v[20:21], v[20:21], 1, s[60:61]
	v_lshl_add_u64 v[20:21], v[20:21], 0, s[4:5]
	v_lshl_add_u64 v[20:21], v[20:21], 0, v[8:9]
	global_store_dwordx4 v[20:21], v[16:19], off
	s_waitcnt lgkmcnt(0)
	s_nop 0
	v_mul_f32_e32 v16, v4, v160
	v_mul_f32_e32 v17, v5, v161
	v_cvt_pk_bf16_f32 v16, v16, v17
	s_waitcnt lgkmcnt(0)
	v_mul_f32_e32 v17, v6, v162
	v_mul_f32_e32 v18, v7, v163
	v_cvt_pk_bf16_f32 v17, v17, v18
	s_waitcnt lgkmcnt(0)
	v_mul_f32_e32 v18, v0, v164
	v_mul_f32_e32 v19, v1, v165
	v_cvt_pk_bf16_f32 v18, v18, v19
	s_waitcnt lgkmcnt(0)
	v_mul_f32_e32 v19, v2, v166
	v_mul_f32_e32 v20, v3, v167
	v_cvt_pk_bf16_f32 v19, v19, v20
	v_add_u32_e32 v20, 32, v24
	v_ashrrev_i32_e32 v21, 31, v20
	v_mul_lo_u32 v22, s56, v21
	v_mul_lo_u32 v23, s57, v20
	v_mad_u64_u32 v[20:21], s[6:7], s56, v20, 0
	v_add3_u32 v21, v21, v22, v23
	v_lshl_add_u64 v[20:21], v[20:21], 1, s[60:61]
	v_lshl_add_u64 v[20:21], v[20:21], 0, s[4:5]
	v_lshl_add_u64 v[20:21], v[20:21], 0, v[8:9]
	global_store_dwordx4 v[20:21], v[16:19], off
	s_waitcnt lgkmcnt(0)
	s_nop 0
	v_mul_f32_e32 v16, v4, v168
	v_mul_f32_e32 v17, v5, v169
	v_cvt_pk_bf16_f32 v16, v16, v17
	s_waitcnt lgkmcnt(0)
	v_mul_f32_e32 v17, v6, v170
	v_mul_f32_e32 v18, v7, v171
	v_cvt_pk_bf16_f32 v17, v17, v18
	s_waitcnt lgkmcnt(0)
	v_mul_f32_e32 v18, v0, v172
	v_mul_f32_e32 v19, v1, v173
	v_cvt_pk_bf16_f32 v18, v18, v19
	s_waitcnt lgkmcnt(0)
	v_mul_f32_e32 v19, v2, v174
	v_mul_f32_e32 v20, v3, v175
	v_cvt_pk_bf16_f32 v19, v19, v20
	v_add_u32_e32 v20, 40, v24
	v_ashrrev_i32_e32 v21, 31, v20
	v_mul_lo_u32 v22, s56, v21
	v_mul_lo_u32 v23, s57, v20
	v_mad_u64_u32 v[20:21], s[6:7], s56, v20, 0
	v_add3_u32 v21, v21, v22, v23
	v_lshl_add_u64 v[20:21], v[20:21], 1, s[60:61]
	v_lshl_add_u64 v[20:21], v[20:21], 0, s[4:5]
	v_lshl_add_u64 v[20:21], v[20:21], 0, v[8:9]
	global_store_dwordx4 v[20:21], v[16:19], off
	s_waitcnt lgkmcnt(0)
	s_nop 0
	v_mul_f32_e32 v16, v4, v176
	v_mul_f32_e32 v17, v5, v177
	v_cvt_pk_bf16_f32 v16, v16, v17
	s_waitcnt lgkmcnt(0)
	v_mul_f32_e32 v17, v6, v178
	v_mul_f32_e32 v18, v7, v179
	v_cvt_pk_bf16_f32 v17, v17, v18
	s_waitcnt lgkmcnt(0)
	v_mul_f32_e32 v18, v0, v180
	v_mul_f32_e32 v19, v1, v181
	v_cvt_pk_bf16_f32 v18, v18, v19
	s_waitcnt lgkmcnt(0)
	v_mul_f32_e32 v19, v2, v182
	v_mul_f32_e32 v20, v3, v183
	v_cvt_pk_bf16_f32 v19, v19, v20
	v_add_u32_e32 v20, 48, v24
	v_ashrrev_i32_e32 v21, 31, v20
	v_mul_lo_u32 v22, s56, v21
	v_mul_lo_u32 v23, s57, v20
	v_mad_u64_u32 v[20:21], s[6:7], s56, v20, 0
	v_add3_u32 v21, v21, v22, v23
	v_lshl_add_u64 v[20:21], v[20:21], 1, s[60:61]
	v_lshl_add_u64 v[20:21], v[20:21], 0, s[4:5]
	v_lshl_add_u64 v[20:21], v[20:21], 0, v[8:9]
	global_store_dwordx4 v[20:21], v[16:19], off
	s_waitcnt lgkmcnt(0)
	v_mul_f32_e32 v4, v4, v184
	v_mul_f32_e32 v5, v5, v185
	v_cvt_pk_bf16_f32 v4, v4, v5
	s_waitcnt lgkmcnt(0)
	v_mul_f32_e32 v5, v6, v186
	v_mul_f32_e32 v6, v7, v187
	v_cvt_pk_bf16_f32 v5, v5, v6
	s_waitcnt lgkmcnt(0)
	v_mul_f32_e32 v0, v0, v188
	v_mul_f32_e32 v1, v1, v189
	v_cvt_pk_bf16_f32 v6, v0, v1
	s_waitcnt lgkmcnt(0)
	v_mul_f32_e32 v0, v2, v190
	v_mul_f32_e32 v1, v3, v191
	v_cvt_pk_bf16_f32 v7, v0, v1
	v_add_u32_e32 v0, 56, v24
	v_ashrrev_i32_e32 v1, 31, v0
	v_mul_lo_u32 v2, s56, v1
	v_mul_lo_u32 v3, s57, v0
	v_mad_u64_u32 v[0:1], s[6:7], s56, v0, 0
	v_add3_u32 v1, v1, v2, v3
	v_lshl_add_u64 v[0:1], v[0:1], 1, s[60:61]
	v_lshl_add_u64 v[0:1], v[0:1], 0, s[4:5]
	v_lshl_add_u64 v[0:1], v[0:1], 0, v[8:9]
	global_store_dwordx4 v[0:1], v[4:7], off
	s_waitcnt lgkmcnt(0)
	s_cbranch_scc0 .Lcvp11_ret
